# P7 gate/up GEMM: wave groups stay staggered through the epilogue (no re-alignment barriers), one extra barrier for group 0 at loop exit
# baseline (speedup 1.0000x reference)
.LBB0_963:
	s_andn2_b64 vcc, exec, s[14:15]
	s_mov_b32 s91, s72
	s_cbranch_vccnz .LBB0_965
	s_nop 0

.LBB0_981:
	s_or_b64 exec, exec, s[0:1]
	s_cmp_eq_u32 s88, s73
	s_mov_b64 s[0:1], -1
	s_cbranch_scc1 .LBB0_925
	v_readlane_b32 s0, v252, 16
	v_readlane_b32 s1, v252, 17
	s_andn2_b64 vcc, exec, s[0:1]
	s_cbranch_vccnz .LBB0_924
	s_nop 0
	s_branch .LBB0_924
.LBB0_984:
	s_waitcnt vmcnt(0)
	s_andn2_b64 vcc, exec, s[14:15]
	s_cbranch_vccnz .Lp7_noxb
	s_barrier
.Lp7_noxb:
	v_readlane_b32 s22, v252, 20
	v_readlane_b32 s90, v252, 13
	v_readlane_b32 s23, v252, 21
	s_barrier
